# v13 without the L2 warm-up loads (sc1 stores only)
# baseline (speedup 1.0000x reference)
.LBB2_414:
	s_movk_i32 s0, 0xc00
	v_mov_b64_e32 v[26:27], s[42:43]
	v_mul_u32_u24_e32 v28, 0xc00, v154
	v_mad_i64_i32 v[26:27], s[0:1], v62, s0, v[26:27]
	v_or_b32_e32 v28, v28, v98
	v_mov_b32_e32 v99, 0
	v_lshl_add_u64 v[26:27], v[26:27], 0, v[98:99]
	v_or_b32_e32 v29, 0x10000, v28
	global_store_dwordx4 v[26:27], v[22:25], off sc1
	ds_write_b128 v29, v[22:25]
	v_sub_f32_e32 v10, v10, v22
	v_or_b32_e32 v22, v101, v154
	v_sub_f32_e32 v11, v11, v23
	v_add_u32_e32 v23, v22, v102
	v_lshl_or_b32 v23, v23, 4, v103
	ds_write_b32 v23, v10
	v_add_u32_e32 v10, v22, v104
	v_lshl_or_b32 v10, v10, 4, v105
	ds_write_b32 v10, v11
	v_or_b32_e32 v10, v106, v154
	v_add_u32_e32 v10, v10, v107
	v_sub_f32_e32 v12, v12, v24
	v_lshl_or_b32 v10, v10, 4, v108
	ds_write_b32 v10, v12
	v_or_b32_e32 v10, v109, v154
	v_add_u32_e32 v10, v10, v110
	v_sub_f32_e32 v13, v13, v25
	v_lshl_or_b32 v10, v10, 4, v111
	ds_write_b32 v10, v13
	v_add_u32_e32 v10, 0x10400, v28
	ds_write_b128 v10, v[18:21]
	v_sub_f32_e32 v10, v6, v18
	v_sub_f32_e32 v11, v7, v19
	v_pk_add_f32 v[6:7], v[8:9], v[20:21] neg_lo:[0,1] neg_hi:[0,1]
	v_or_b32_e32 v8, v112, v154
	v_add_u32_e32 v9, v8, v113
	v_add_u32_e32 v8, v8, v115
	v_lshl_or_b32 v9, v9, 4, v114
	v_lshl_or_b32 v8, v8, 4, v116
	ds_write_b32 v9, v10
	ds_write_b32 v8, v11
	v_or_b32_e32 v8, v117, v154
	v_add_u32_e32 v8, v8, v118
	v_lshl_or_b32 v8, v8, 4, v119
	ds_write_b32 v8, v6
	v_or_b32_e32 v6, v120, v154
	v_add_u32_e32 v6, v6, v121
	v_lshl_or_b32 v6, v6, 4, v122
	ds_write_b32 v6, v7
	v_add_u32_e32 v6, 0x10800, v28
	ds_write_b128 v6, v[14:17]
	v_or_b32_e32 v6, v123, v154
	v_add_u32_e32 v7, v6, v124
	v_pk_add_f32 v[2:3], v[2:3], v[14:15] neg_lo:[0,1] neg_hi:[0,1]
	v_lshl_or_b32 v7, v7, 4, v125
	ds_write_b32 v7, v2
	v_add_u32_e32 v2, v6, v126
	v_lshl_or_b32 v2, v2, 4, v127
	ds_write_b32 v2, v3
	v_or_b32_e32 v2, v133, v154
	v_add_u32_e32 v2, v2, v134
	v_pk_add_f32 v[4:5], v[4:5], v[16:17] neg_lo:[0,1] neg_hi:[0,1]
	v_lshl_or_b32 v2, v2, 4, v63
	ds_write_b32 v2, v4
	v_or_b32_e32 v2, v135, v154
	v_add_u32_e32 v2, v2, v132
	v_lshl_or_b32 v2, v2, 4, v136
	v_add_lshl_u32 v4, v100, v154, 4
	s_mov_b32 s5, 0
	s_mov_b32 s4, 1.0
	ds_write_b32 v2, v5
	v_mov_b64_e32 v[2:3], s[4:5]
	v_add_u32_e32 v4, 8, v4
	s_waitcnt vmcnt(1)
	v_lshlrev_b32_e32 v40, 9, v150
	ds_write2st64_b64 v4, v[2:3], v[2:3] offset1:64
	v_or_b32_e32 v2, v40, v128
	v_lshlrev_b32_e32 v98, 4, v2
	v_lshl_add_u64 v[100:101], s[40:41], 0, v[98:99]
	s_mov_b64 s[0:1], 0x787000
	v_lshl_add_u64 v[34:35], v[100:101], 0, s[0:1]
	s_mov_b32 s0, 0x788000
	v_add_co_u32_e32 v36, vcc, s0, v100
	global_store_dwordx4 v[26:27], v[18:21], off offset:1024 sc1
	global_store_dwordx4 v[26:27], v[14:17], off offset:2048 sc1
	s_waitcnt lgkmcnt(0)
	s_barrier
	v_addc_co_u32_e32 v37, vcc, 0, v101, vcc
	global_load_dwordx4 v[2:5], v[34:35], off offset:1024
	global_load_dwordx4 v[10:13], v[34:35], off offset:2048
	global_load_dwordx4 v[14:17], v[34:35], off offset:3072
	global_load_dwordx4 v[6:9], v[36:37], off offset:-4096
	global_load_dwordx4 v[18:21], v[36:37], off
	global_load_dwordx4 v[22:25], v[36:37], off offset:1024
	global_load_dwordx4 v[26:29], v[36:37], off offset:2048
	global_load_dwordx4 v[30:33], v[36:37], off offset:3072
	v_and_b32_e32 v35, 15, v0
	v_lshrrev_b32_e32 v37, 4, v128
	v_lshlrev_b32_e32 v102, 2, v35
	v_lshlrev_b32_e32 v41, 2, v37
	v_lshlrev_b32_e32 v34, 4, v35
	v_cmp_gt_u32_e64 s[0:1], 6, v35
	v_mov_b32_e32 v35, v99
	v_or3_b32 v36, v34, v41, v40
	v_lshl_add_u64 v[104:105], s[44:45], 0, v[34:35]
	v_or_b32_e32 v34, v40, v34
	s_movk_i32 s4, 0x1000
	v_or3_b32 v153, v34, v41, s4
	v_or_b32_e32 v34, 0x11800, v98
	v_lshl_add_u64 v[118:119], s[40:41], 0, v[34:35]
	v_or_b32_e32 v34, 0x11400, v98
	v_lshl_add_u64 v[120:121], s[40:41], 0, v[34:35]
	v_or_b32_e32 v34, 0x11000, v98
	ds_read2st64_b32 v[132:133], v36 offset1:1
	v_or_b32_e32 v36, s33, v41
	v_lshl_add_u64 v[122:123], s[40:41], 0, v[34:35]
	v_or_b32_e32 v34, 0x10c00, v98
	v_or_b32_e32 v38, 1, v36
	v_lshl_add_u64 v[124:125], s[40:41], 0, v[34:35]
	v_or_b32_e32 v34, 0x10800, v98
	v_mul_u32_u24_e32 v152, 0x3000, v37
	v_ashrrev_i32_e32 v37, 31, v36
	v_ashrrev_i32_e32 v39, 31, v38
	v_lshl_add_u64 v[126:127], s[40:41], 0, v[34:35]
	v_or_b32_e32 v34, 0x10400, v98
	v_mov_b32_e32 v103, v99
	v_lshlrev_b64 v[108:109], 17, v[36:37]
	v_lshlrev_b64 v[110:111], 17, v[38:39]
	v_or_b32_e32 v38, 2, v36
	v_or_b32_e32 v36, 3, v36
	v_lshl_add_u64 v[128:129], s[40:41], 0, v[34:35]
	v_mul_u32_u24_e32 v34, 24, v150
	v_lshl_add_u64 v[106:107], s[38:39], 0, v[102:103]
	v_ashrrev_i32_e32 v39, 31, v38
	v_ashrrev_i32_e32 v37, 31, v36
	v_lshlrev_b32_e32 v103, 2, v0
	v_or_b32_e32 v98, 0x11c00, v98
	v_or_b32_e32 v34, v152, v34
	v_lshlrev_b64 v[112:113], 17, v[38:39]
	v_lshlrev_b64 v[114:115], 17, v[36:37]
	v_and_b32_e32 v116, 0x700, v103
	v_mov_b32_e32 v117, v99
	v_lshl_add_u64 v[130:131], s[40:41], 0, v[98:99]
	v_add_u32_e32 v154, v34, v102
	s_mov_b64 s[6:7], 0
	s_mov_b64 s[8:9], 0x800
	v_mov_b32_e32 v155, 0x400
	v_mov_b32_e32 v159, 0
	v_mov_b32_e32 v158, 0
	v_mov_b32_e32 v157, 0
	v_mov_b32_e32 v156, 0
	v_readfirstlane_b32 s78, v150
	v_and_b32_e32 v104, 63, v0
	v_lshlrev_b32_e32 v104, 4, v104
	v_lshl_or_b32 v104, v150, 13, v104
	v_add_u32_e32 v105, 0xfffff000, v153
	v_mov_b32_e32 v106, v154
	v_lshrrev_b32_e32 v98, 2, v102
	v_cmp_gt_u32_e32 vcc, 6, v98
	v_add_u32_e32 v107, -6, v98
	s_nop 0
	v_cndmask_b32_e32 v107, v107, v98, vcc
	v_cmp_gt_u32_e32 vcc, 6, v107
	v_add_u32_e32 v98, -6, v107
	s_nop 0
	v_cndmask_b32_e32 v107, v98, v107, vcc
	v_lshlrev_b32_e32 v107, 2, v107
	v_sub_u32_e32 v106, v106, v102
	v_add_u32_e32 v106, v106, v107
	v_and_b32_e32 v98, 63, v0
	v_lshrrev_b32_e32 v98, 4, v98
	v_lshlrev_b32_e32 v98, 19, v98
	v_lshl_or_b32 v108, v102, 2, v98
	v_add_u32_e32 v109, 0x20000, v108
	v_add_u32_e32 v110, 0x40000, v108
	v_add_u32_e32 v111, 0x60000, v108
	v_mov_b32_e32 v240, 0
	v_mov_b32_e32 v241, 0
	v_mov_b32_e32 v242, 0
	v_mov_b32_e32 v243, 0
	s_lshl_b32 s84, s33, 17
	s_lshl_b32 s85, s78, 10
	s_add_u32 s84, s84, s85
	s_add_u32 s80, s44, s84
	s_addc_u32 s81, s45, 0
	s_mul_i32 s84, s78, 0x1800
	s_add_u32 s94, s38, s84
	s_addc_u32 s95, s39, 0
	s_mov_b32 s70, 0
	s_add_u32 s86, s40, 0x797000
	s_addc_u32 s87, s41, 0
	s_add_u32 s88, s86, 0x1000
	s_addc_u32 s89, s87, 0
	v_add_u32_e32 v112, 0x1000, v105
	s_waitcnt vmcnt(0) lgkmcnt(0)
	v_mfma_f32_16x16x4_f32 v[34:37], v132, v6, 0
	v_mfma_f32_16x16x4_f32 v[38:41], v132, v8, 0
	v_mfma_f32_16x16x4_f32 v[34:37], v133, v7, v[34:37]
	v_mfma_f32_16x16x4_f32 v[38:41], v133, v9, v[38:41]
	global_load_dwordx4 v[6:9], v104, s[86:87]
	v_mfma_f32_16x16x4_f32 v[42:45], v132, v2, 0
	v_mfma_f32_16x16x4_f32 v[46:49], v132, v4, 0
	v_mfma_f32_16x16x4_f32 v[42:45], v133, v3, v[42:45]
	v_mfma_f32_16x16x4_f32 v[46:49], v133, v5, v[46:49]
	global_load_dwordx4 v[2:5], v104, s[86:87] offset:1024
	v_mfma_f32_16x16x4_f32 v[50:53], v132, v10, 0
	v_mfma_f32_16x16x4_f32 v[54:57], v132, v12, 0
	v_mfma_f32_16x16x4_f32 v[50:53], v133, v11, v[50:53]
	v_mfma_f32_16x16x4_f32 v[54:57], v133, v13, v[54:57]
	global_load_dwordx4 v[10:13], v104, s[86:87] offset:2048
	v_mfma_f32_16x16x4_f32 v[58:61], v132, v14, 0
	v_mfma_f32_16x16x4_f32 v[62:65], v132, v16, 0
	v_mfma_f32_16x16x4_f32 v[58:61], v133, v15, v[58:61]
	v_mfma_f32_16x16x4_f32 v[62:65], v133, v17, v[62:65]
	global_load_dwordx4 v[14:17], v104, s[86:87] offset:3072
	v_mfma_f32_16x16x4_f32 v[66:69], v132, v18, 0
	v_mfma_f32_16x16x4_f32 v[70:73], v132, v20, 0
	v_mfma_f32_16x16x4_f32 v[66:69], v133, v19, v[66:69]
	v_mfma_f32_16x16x4_f32 v[70:73], v133, v21, v[70:73]
	global_load_dwordx4 v[18:21], v104, s[88:89]
	v_mfma_f32_16x16x4_f32 v[74:77], v132, v22, 0
	v_mfma_f32_16x16x4_f32 v[78:81], v132, v24, 0
	v_mfma_f32_16x16x4_f32 v[74:77], v133, v23, v[74:77]
	v_mfma_f32_16x16x4_f32 v[78:81], v133, v25, v[78:81]
	global_load_dwordx4 v[22:25], v104, s[88:89] offset:1024
	v_mfma_f32_16x16x4_f32 v[82:85], v132, v26, 0
	v_mfma_f32_16x16x4_f32 v[86:89], v132, v28, 0
	v_mfma_f32_16x16x4_f32 v[82:85], v133, v27, v[82:85]
	v_mfma_f32_16x16x4_f32 v[86:89], v133, v29, v[86:89]
	global_load_dwordx4 v[26:29], v104, s[88:89] offset:2048
	v_mfma_f32_16x16x4_f32 v[90:93], v132, v30, 0
	v_mfma_f32_16x16x4_f32 v[94:97], v132, v32, 0
	v_mfma_f32_16x16x4_f32 v[90:93], v133, v31, v[90:93]
	v_mfma_f32_16x16x4_f32 v[94:97], v133, v33, v[94:97]
	global_load_dwordx4 v[30:33], v104, s[88:89] offset:3072
	ds_read2st64_b32 v[132:133], v112 offset1:1
	s_nop 7
	s_nop 7
	v_max3_f32 v114, v34, v38, v42
	v_max3_f32 v116, v46, v50, v54
	v_max3_f32 v114, v114, v58, v62
	v_max3_f32 v116, v116, v66, v70
	v_max3_f32 v114, v114, v74, v78
	v_max3_f32 v116, v116, v82, v86
	v_max3_f32 v114, v114, v90, v94
	v_max_f32_e32 v114, v114, v116
	s_nop 1
	v_max_f32_dpp v114, v114, v114 row_ror:1 row_mask:0xf bank_mask:0xf
	s_nop 1
	v_max_f32_dpp v114, v114, v114 row_ror:2 row_mask:0xf bank_mask:0xf
	s_nop 1
	v_max_f32_dpp v114, v114, v114 row_ror:4 row_mask:0xf bank_mask:0xf
	s_nop 1
	v_max_f32_dpp v114, v114, v114 row_ror:8 row_mask:0xf bank_mask:0xf
	s_waitcnt vmcnt(0) lgkmcnt(0)
